# agg1: fixed softmax reference (first-stage max) with overflow-guarded out-of-line rescale instead of per-stage running-max rescale
# baseline (speedup 1.0000x reference)
_Z11agg1_kernelPKDF16_PKfS2_PKiS4_S2_S2_PDF16_PfS6_i:
	s_load_dwordx8 s[4:11], s[0:1], 0x0
	s_load_dwordx8 s[12:19], s[0:1], 0x20
	s_load_dwordx4 s[20:23], s[0:1], 0x40
	s_load_dword s24, s[0:1], 0x50
	v_lshlrev_b32_e32 v32, 2, v0
	v_readfirstlane_b32 s25, v0
	s_lshl_b32 s26, s2, 5
	v_and_b32_e32 v64, 7, v0
	v_bfe_u32 v65, v0, 3, 3
	v_and_b32_e32 v45, 31, v0
	s_lshr_b32 s25, s25, 6
	v_lshlrev_b32_e32 v1, 1, v64
	v_add_u32_e32 v46, s26, v45
	s_waitcnt lgkmcnt(0)
	global_load_dword v33, v32, s[14:15]
	global_load_dword v34, v32, s[16:17]
	s_add_i32 s28, s24, -1
	v_cmp_gt_i32_e64 s[38:39], s24, v46
	v_min_i32_e32 v46, s28, v46
	v_lshlrev_b32_e32 v47, 2, v46
	global_load_dword v44, v47, s[10:11]
	global_load_dword v48, v47, s[10:11] offset:4
	s_lshl_b32 s27, s25, 11
	v_lshlrev_b32_e32 v62, 6, v64
	v_add_u32_e32 v62, 0x2000, v62
	v_cmp_eq_u32_e64 s[34:35], 0, v64
	v_lshlrev_b32_e32 v35, 8, v64
	v_lshl_add_u32 v35, v65, 4, v35
	v_add_u32_e32 v63, s27, v35
	v_mov_b32_e32 v36, 0
	v_mov_b32_e32 v37, 0
	v_mov_b32_e32 v38, 0
	v_mov_b32_e32 v39, 0
	s_waitcnt vmcnt(2)
	ds_write2st64_b32 v32, v33, v34 offset0:32 offset1:36
	ds_write_b128 v63, v[36:39]
	ds_write_b128 v63, v[36:39] offset:128
	s_waitcnt vmcnt(0)
	v_sub_u32_e32 v48, v48, v44
	v_add_u32_e32 v48, 1, v48
	v_cndmask_b32_e64 v48, 0, v48, s[38:39]
	v_lshl_or_b32 v40, v48, 5, v45
	s_nop 1
	v_mov_b32_dpp v41, v40 quad_perm:[1,0,3,2] row_mask:0xf bank_mask:0xf
	s_mov_b32 s40, 0x99999999
	s_mov_b32 s41, 0x99999999
	v_min_u32_e32 v42, v40, v41
	v_max_u32_e32 v43, v40, v41
	v_cndmask_b32_e64 v40, v42, v43, s[40:41]
	s_nop 1
	v_mov_b32_dpp v41, v40 quad_perm:[2,3,0,1] row_mask:0xf bank_mask:0xf
	s_mov_b32 s40, 0xc3c3c3c3
	s_mov_b32 s41, 0xc3c3c3c3
	v_min_u32_e32 v42, v40, v41
	v_max_u32_e32 v43, v40, v41
	v_cndmask_b32_e64 v40, v42, v43, s[40:41]
	s_nop 1
	v_mov_b32_dpp v41, v40 quad_perm:[1,0,3,2] row_mask:0xf bank_mask:0xf
	s_mov_b32 s40, 0xa5a5a5a5
	s_mov_b32 s41, 0xa5a5a5a5
	v_min_u32_e32 v42, v40, v41
	v_max_u32_e32 v43, v40, v41
	v_cndmask_b32_e64 v40, v42, v43, s[40:41]
	ds_swizzle_b32 v41, v40 offset:swizzle(SWAP,4)
	s_waitcnt lgkmcnt(0)
	s_mov_b32 s40, 0xf00ff00f
	s_mov_b32 s41, 0xf00ff00f
	v_min_u32_e32 v42, v40, v41
	v_max_u32_e32 v43, v40, v41
	v_cndmask_b32_e64 v40, v42, v43, s[40:41]
	s_nop 1
	v_mov_b32_dpp v41, v40 quad_perm:[2,3,0,1] row_mask:0xf bank_mask:0xf
	s_mov_b32 s40, 0xcc33cc33
	s_mov_b32 s41, 0xcc33cc33
	v_min_u32_e32 v42, v40, v41
	v_max_u32_e32 v43, v40, v41
	v_cndmask_b32_e64 v40, v42, v43, s[40:41]
	s_nop 1
	v_mov_b32_dpp v41, v40 quad_perm:[1,0,3,2] row_mask:0xf bank_mask:0xf
	s_mov_b32 s40, 0xaa55aa55
	s_mov_b32 s41, 0xaa55aa55
	v_min_u32_e32 v42, v40, v41
	v_max_u32_e32 v43, v40, v41
	v_cndmask_b32_e64 v40, v42, v43, s[40:41]
	ds_swizzle_b32 v41, v40 offset:swizzle(SWAP,8)
	s_waitcnt lgkmcnt(0)
	s_mov_b32 s40, 0xff0000ff
	s_mov_b32 s41, 0xff0000ff
	v_min_u32_e32 v42, v40, v41
	v_max_u32_e32 v43, v40, v41
	v_cndmask_b32_e64 v40, v42, v43, s[40:41]
	ds_swizzle_b32 v41, v40 offset:swizzle(SWAP,4)
	s_waitcnt lgkmcnt(0)
	s_mov_b32 s40, 0xf0f00f0f
	s_mov_b32 s41, 0xf0f00f0f
	v_min_u32_e32 v42, v40, v41
	v_max_u32_e32 v43, v40, v41
	v_cndmask_b32_e64 v40, v42, v43, s[40:41]
	s_nop 1
	v_mov_b32_dpp v41, v40 quad_perm:[2,3,0,1] row_mask:0xf bank_mask:0xf
	s_mov_b32 s40, 0xcccc3333
	s_mov_b32 s41, 0xcccc3333
	v_min_u32_e32 v42, v40, v41
	v_max_u32_e32 v43, v40, v41
	v_cndmask_b32_e64 v40, v42, v43, s[40:41]
	s_nop 1
	v_mov_b32_dpp v41, v40 quad_perm:[1,0,3,2] row_mask:0xf bank_mask:0xf
	s_mov_b32 s40, 0xaaaa5555
	s_mov_b32 s41, 0xaaaa5555
	v_min_u32_e32 v42, v40, v41
	v_max_u32_e32 v43, v40, v41
	v_cndmask_b32_e64 v40, v42, v43, s[40:41]
	ds_swizzle_b32 v41, v40 offset:swizzle(SWAP,16)
	s_waitcnt lgkmcnt(0)
	s_mov_b32 s40, 0xffff
	s_mov_b32 s41, 0xffff
	v_min_u32_e32 v42, v40, v41
	v_max_u32_e32 v43, v40, v41
	v_cndmask_b32_e64 v40, v42, v43, s[40:41]
	ds_swizzle_b32 v41, v40 offset:swizzle(SWAP,8)
	s_waitcnt lgkmcnt(0)
	s_mov_b32 s40, 0xff00ff
	s_mov_b32 s41, 0xff00ff
	v_min_u32_e32 v42, v40, v41
	v_max_u32_e32 v43, v40, v41
	v_cndmask_b32_e64 v40, v42, v43, s[40:41]
	ds_swizzle_b32 v41, v40 offset:swizzle(SWAP,4)
	s_waitcnt lgkmcnt(0)
	s_mov_b32 s40, 0xf0f0f0f
	s_mov_b32 s41, 0xf0f0f0f
	v_min_u32_e32 v42, v40, v41
	v_max_u32_e32 v43, v40, v41
	v_cndmask_b32_e64 v40, v42, v43, s[40:41]
	s_nop 1
	v_mov_b32_dpp v41, v40 quad_perm:[2,3,0,1] row_mask:0xf bank_mask:0xf
	s_mov_b32 s40, 0x33333333
	s_mov_b32 s41, 0x33333333
	v_min_u32_e32 v42, v40, v41
	v_max_u32_e32 v43, v40, v41
	v_cndmask_b32_e64 v40, v42, v43, s[40:41]
	s_nop 1
	v_mov_b32_dpp v41, v40 quad_perm:[1,0,3,2] row_mask:0xf bank_mask:0xf
	s_mov_b32 s40, 0x55555555
	s_mov_b32 s41, 0x55555555
	v_min_u32_e32 v42, v40, v41
	v_max_u32_e32 v43, v40, v41
	v_cndmask_b32_e64 v40, v42, v43, s[40:41]
	s_lshl_b32 s40, s25, 3
	v_add_u32_e32 v45, s40, v65
	v_lshlrev_b32_e32 v45, 2, v45
	ds_bpermute_b32 v46, v45, v40
	s_waitcnt lgkmcnt(0)
	v_and_b32_e32 v15, 31, v46
	v_lshrrev_b32_e32 v11, 5, v46
	v_lshlrev_b32_e32 v47, 2, v15
	ds_bpermute_b32 v10, v47, v44
	v_add_u32_e32 v66, s26, v15
	v_min_i32_e32 v66, s28, v66
	v_cmp_lt_u32_e64 s[36:37], 0, v11
	v_lshlrev_b32_e32 v4, 2, v66
	v_lshlrev_b32_e32 v35, 2, v64
	v_lshl_or_b32 v35, v66, 5, v35
	global_load_dword v9, v35, s[8:9]
	v_lshrrev_b32_e32 v3, 3, v15
	v_lshlrev_b32_e32 v3, 11, v3
	v_and_b32_e32 v47, 7, v15
	v_lshl_add_u32 v3, v47, 1, v3
	v_lshl_add_u32 v3, v64, 4, v3
	v_readfirstlane_b32 s29, v11
	s_waitcnt lgkmcnt(0)
	s_barrier
	v_add_u32_e32 v67, v10, v64
	v_lshlrev_b32_e32 v67, 2, v67
	v_mov_b32_e32 v5, s24
	v_mov_b32_e32 v6, s24
	v_mov_b32_e32 v7, s24
	v_mov_b32_e32 v8, s24
	v_mov_b32_e32 v69, s24
	v_cndmask_b32_e64 v5, v5, v66, s[34:35]
	v_cmp_gt_i32_e32 vcc, v11, v64
	s_andn2_b64 s[40:41], vcc, s[34:35]
	s_and_saveexec_b64 s[32:33], s[40:41]
	global_load_dword v5, v67, s[12:13] offset:-4
	s_mov_b64 exec, s[32:33]
	v_add_u32_e32 v68, 8, v64
	v_cmp_gt_i32_e32 vcc, v11, v68
	s_and_saveexec_b64 s[32:33], vcc
	global_load_dword v6, v67, s[12:13] offset:28
	s_mov_b64 exec, s[32:33]
	v_add_u32_e32 v68, 16, v64
	v_cmp_gt_i32_e32 vcc, v11, v68
	s_and_saveexec_b64 s[32:33], vcc
	global_load_dword v7, v67, s[12:13] offset:60
	s_mov_b64 exec, s[32:33]
	v_add_u32_e32 v68, 24, v64
	v_cmp_gt_i32_e32 vcc, v11, v68
	s_and_saveexec_b64 s[32:33], vcc
	global_load_dword v8, v67, s[12:13] offset:92
	s_mov_b64 exec, s[32:33]
	v_add_u32_e32 v68, 32, v64
	v_cmp_gt_i32_e32 vcc, v11, v68
	s_and_saveexec_b64 s[32:33], vcc
	global_load_dword v69, v67, s[12:13] offset:124
	s_mov_b64 exec, s[32:33]
	s_waitcnt vmcnt(0)
	v_lshlrev_b32_e32 v5, 4, v5
	v_lshlrev_b32_e32 v6, 4, v6
	v_lshlrev_b32_e32 v7, 4, v7
	v_lshlrev_b32_e32 v8, 4, v8
	v_lshlrev_b32_e32 v69, 4, v69
	s_mov_b32 s42, 0
	s_mov_b32 s43, 0
	s_cmp_lt_i32 s29, 3
	s_cbranch_scc1 .Lagg_first_half
	ds_swizzle_b32 v32, v5 offset:swizzle(BITMASK_PERM, "pp000")
	ds_swizzle_b32 v33, v5 offset:swizzle(BITMASK_PERM, "pp001")
	ds_swizzle_b32 v34, v5 offset:swizzle(BITMASK_PERM, "pp010")
	ds_swizzle_b32 v35, v5 offset:swizzle(BITMASK_PERM, "pp011")
	s_waitcnt lgkmcnt(0)
	v_or_b32_e32 v32, v32, v1
	v_or_b32_e32 v33, v33, v1
	v_or_b32_e32 v34, v34, v1
	v_or_b32_e32 v35, v35, v1
	global_load_ushort v36, v32, s[6:7]
	global_load_ushort v37, v33, s[6:7]
	global_load_ushort v38, v34, s[6:7]
	global_load_ushort v39, v35, s[6:7]
	v_lshlrev_b32_e32 v32, 3, v32
	v_lshlrev_b32_e32 v33, 3, v33
	v_lshlrev_b32_e32 v34, 3, v34
	v_lshlrev_b32_e32 v35, 3, v35
	global_load_dwordx4 v[40:43], v32, s[4:5]
	global_load_dwordx4 v[44:47], v33, s[4:5]
	global_load_dwordx4 v[48:51], v34, s[4:5]
	global_load_dwordx4 v[52:55], v35, s[4:5]
	s_waitcnt vmcnt(4)
	v_fma_mix_f32 v36, v36, 1.0, v9 op_sel_hi:[1,0,0]
	v_fma_mix_f32 v37, v37, 1.0, v9 op_sel_hi:[1,0,0]
	v_fma_mix_f32 v38, v38, 1.0, v9 op_sel_hi:[1,0,0]
	v_fma_mix_f32 v39, v39, 1.0, v9 op_sel_hi:[1,0,0]
	v_mul_f32_e32 v58, 0x3e4ccccd, v36
	v_mul_f32_e32 v59, 0x3e4ccccd, v37
	v_mul_f32_e32 v60, 0x3e4ccccd, v38
	v_mul_f32_e32 v61, 0x3e4ccccd, v39
	v_max_f32_e32 v36, v36, v58
	v_max_f32_e32 v37, v37, v59
	v_max_f32_e32 v38, v38, v60
	v_max_f32_e32 v39, v39, v61
	v_max3_f32 v56, v36, v37, v38
	v_max_f32_e32 v13, v56, v39
	v_sub_f32_e32 v36, v36, v13
	v_sub_f32_e32 v37, v37, v13
	v_sub_f32_e32 v38, v38, v13
	v_sub_f32_e32 v39, v39, v13
	v_exp_f32_e32 v36, v36
	v_exp_f32_e32 v37, v37
	v_exp_f32_e32 v38, v38
	v_exp_f32_e32 v39, v39
	s_nop 0
	v_add_f32_e32 v14, v36, v37
	v_add_f32_e32 v14, v14, v38
	v_add_f32_e32 v14, v14, v39
	s_waitcnt vmcnt(3)
	v_cvt_scalef32_pk_f16_fp8 v58, v40, 1.0
	v_cvt_scalef32_pk_f16_fp8 v59, v40, 1.0 op_sel:[1,0,0]
	v_cvt_scalef32_pk_f16_fp8 v60, v41, 1.0
	v_cvt_scalef32_pk_f16_fp8 v61, v41, 1.0 op_sel:[1,0,0]
	v_fma_mix_f32 v16, v58, v36, 0 op_sel_hi:[1,0,0]
	v_fma_mix_f32 v17, v58, v36, 0 op_sel:[1,0,0] op_sel_hi:[1,0,0]
	v_fma_mix_f32 v18, v59, v36, 0 op_sel_hi:[1,0,0]
	v_fma_mix_f32 v19, v59, v36, 0 op_sel:[1,0,0] op_sel_hi:[1,0,0]
	v_fma_mix_f32 v20, v60, v36, 0 op_sel_hi:[1,0,0]
	v_fma_mix_f32 v21, v60, v36, 0 op_sel:[1,0,0] op_sel_hi:[1,0,0]
	v_fma_mix_f32 v22, v61, v36, 0 op_sel_hi:[1,0,0]
	v_fma_mix_f32 v23, v61, v36, 0 op_sel:[1,0,0] op_sel_hi:[1,0,0]
	v_cvt_scalef32_pk_f16_fp8 v58, v42, 1.0
	v_cvt_scalef32_pk_f16_fp8 v59, v42, 1.0 op_sel:[1,0,0]
	v_cvt_scalef32_pk_f16_fp8 v60, v43, 1.0
	v_cvt_scalef32_pk_f16_fp8 v61, v43, 1.0 op_sel:[1,0,0]
	v_fma_mix_f32 v24, v58, v36, 0 op_sel_hi:[1,0,0]
	v_fma_mix_f32 v25, v58, v36, 0 op_sel:[1,0,0] op_sel_hi:[1,0,0]
	v_fma_mix_f32 v26, v59, v36, 0 op_sel_hi:[1,0,0]
	v_fma_mix_f32 v27, v59, v36, 0 op_sel:[1,0,0] op_sel_hi:[1,0,0]
	v_fma_mix_f32 v28, v60, v36, 0 op_sel_hi:[1,0,0]
	v_fma_mix_f32 v29, v60, v36, 0 op_sel:[1,0,0] op_sel_hi:[1,0,0]
	v_fma_mix_f32 v30, v61, v36, 0 op_sel_hi:[1,0,0]
	v_fma_mix_f32 v31, v61, v36, 0 op_sel:[1,0,0] op_sel_hi:[1,0,0]
	s_waitcnt vmcnt(2)
	v_cvt_scalef32_pk_f16_fp8 v58, v44, 1.0
	v_cvt_scalef32_pk_f16_fp8 v59, v44, 1.0 op_sel:[1,0,0]
	v_cvt_scalef32_pk_f16_fp8 v60, v45, 1.0
	v_cvt_scalef32_pk_f16_fp8 v61, v45, 1.0 op_sel:[1,0,0]
	v_fma_mix_f32 v16, v58, v37, v16 op_sel_hi:[1,0,0]
	v_fma_mix_f32 v17, v58, v37, v17 op_sel:[1,0,0] op_sel_hi:[1,0,0]
	v_fma_mix_f32 v18, v59, v37, v18 op_sel_hi:[1,0,0]
	v_fma_mix_f32 v19, v59, v37, v19 op_sel:[1,0,0] op_sel_hi:[1,0,0]
	v_fma_mix_f32 v20, v60, v37, v20 op_sel_hi:[1,0,0]
	v_fma_mix_f32 v21, v60, v37, v21 op_sel:[1,0,0] op_sel_hi:[1,0,0]
	v_fma_mix_f32 v22, v61, v37, v22 op_sel_hi:[1,0,0]
	v_fma_mix_f32 v23, v61, v37, v23 op_sel:[1,0,0] op_sel_hi:[1,0,0]
	v_cvt_scalef32_pk_f16_fp8 v58, v46, 1.0
	v_cvt_scalef32_pk_f16_fp8 v59, v46, 1.0 op_sel:[1,0,0]
	v_cvt_scalef32_pk_f16_fp8 v60, v47, 1.0
	v_cvt_scalef32_pk_f16_fp8 v61, v47, 1.0 op_sel:[1,0,0]
	v_fma_mix_f32 v24, v58, v37, v24 op_sel_hi:[1,0,0]
	v_fma_mix_f32 v25, v58, v37, v25 op_sel:[1,0,0] op_sel_hi:[1,0,0]
	v_fma_mix_f32 v26, v59, v37, v26 op_sel_hi:[1,0,0]
	v_fma_mix_f32 v27, v59, v37, v27 op_sel:[1,0,0] op_sel_hi:[1,0,0]
	v_fma_mix_f32 v28, v60, v37, v28 op_sel_hi:[1,0,0]
	v_fma_mix_f32 v29, v60, v37, v29 op_sel:[1,0,0] op_sel_hi:[1,0,0]
	v_fma_mix_f32 v30, v61, v37, v30 op_sel_hi:[1,0,0]
	v_fma_mix_f32 v31, v61, v37, v31 op_sel:[1,0,0] op_sel_hi:[1,0,0]
	s_waitcnt vmcnt(1)
	v_cvt_scalef32_pk_f16_fp8 v58, v48, 1.0
	v_cvt_scalef32_pk_f16_fp8 v59, v48, 1.0 op_sel:[1,0,0]
	v_cvt_scalef32_pk_f16_fp8 v60, v49, 1.0
	v_cvt_scalef32_pk_f16_fp8 v61, v49, 1.0 op_sel:[1,0,0]
	v_fma_mix_f32 v16, v58, v38, v16 op_sel_hi:[1,0,0]
	v_fma_mix_f32 v17, v58, v38, v17 op_sel:[1,0,0] op_sel_hi:[1,0,0]
	v_fma_mix_f32 v18, v59, v38, v18 op_sel_hi:[1,0,0]
	v_fma_mix_f32 v19, v59, v38, v19 op_sel:[1,0,0] op_sel_hi:[1,0,0]
	v_fma_mix_f32 v20, v60, v38, v20 op_sel_hi:[1,0,0]
	v_fma_mix_f32 v21, v60, v38, v21 op_sel:[1,0,0] op_sel_hi:[1,0,0]
	v_fma_mix_f32 v22, v61, v38, v22 op_sel_hi:[1,0,0]
	v_fma_mix_f32 v23, v61, v38, v23 op_sel:[1,0,0] op_sel_hi:[1,0,0]
	v_cvt_scalef32_pk_f16_fp8 v58, v50, 1.0
	v_cvt_scalef32_pk_f16_fp8 v59, v50, 1.0 op_sel:[1,0,0]
	v_cvt_scalef32_pk_f16_fp8 v60, v51, 1.0
	v_cvt_scalef32_pk_f16_fp8 v61, v51, 1.0 op_sel:[1,0,0]
	v_fma_mix_f32 v24, v58, v38, v24 op_sel_hi:[1,0,0]
	v_fma_mix_f32 v25, v58, v38, v25 op_sel:[1,0,0] op_sel_hi:[1,0,0]
	v_fma_mix_f32 v26, v59, v38, v26 op_sel_hi:[1,0,0]
	v_fma_mix_f32 v27, v59, v38, v27 op_sel:[1,0,0] op_sel_hi:[1,0,0]
	v_fma_mix_f32 v28, v60, v38, v28 op_sel_hi:[1,0,0]
	v_fma_mix_f32 v29, v60, v38, v29 op_sel:[1,0,0] op_sel_hi:[1,0,0]
	v_fma_mix_f32 v30, v61, v38, v30 op_sel_hi:[1,0,0]
	v_fma_mix_f32 v31, v61, v38, v31 op_sel:[1,0,0] op_sel_hi:[1,0,0]
	s_waitcnt vmcnt(0)
	v_cvt_scalef32_pk_f16_fp8 v58, v52, 1.0
	v_cvt_scalef32_pk_f16_fp8 v59, v52, 1.0 op_sel:[1,0,0]
	v_cvt_scalef32_pk_f16_fp8 v60, v53, 1.0
	v_cvt_scalef32_pk_f16_fp8 v61, v53, 1.0 op_sel:[1,0,0]
	v_fma_mix_f32 v16, v58, v39, v16 op_sel_hi:[1,0,0]
	v_fma_mix_f32 v17, v58, v39, v17 op_sel:[1,0,0] op_sel_hi:[1,0,0]
	v_fma_mix_f32 v18, v59, v39, v18 op_sel_hi:[1,0,0]
	v_fma_mix_f32 v19, v59, v39, v19 op_sel:[1,0,0] op_sel_hi:[1,0,0]
	v_fma_mix_f32 v20, v60, v39, v20 op_sel_hi:[1,0,0]
	v_fma_mix_f32 v21, v60, v39, v21 op_sel:[1,0,0] op_sel_hi:[1,0,0]
	v_fma_mix_f32 v22, v61, v39, v22 op_sel_hi:[1,0,0]
	v_fma_mix_f32 v23, v61, v39, v23 op_sel:[1,0,0] op_sel_hi:[1,0,0]
	v_cvt_scalef32_pk_f16_fp8 v58, v54, 1.0
	v_cvt_scalef32_pk_f16_fp8 v59, v54, 1.0 op_sel:[1,0,0]
	v_cvt_scalef32_pk_f16_fp8 v60, v55, 1.0
	v_cvt_scalef32_pk_f16_fp8 v61, v55, 1.0 op_sel:[1,0,0]
	v_fma_mix_f32 v24, v58, v39, v24 op_sel_hi:[1,0,0]
	v_fma_mix_f32 v25, v58, v39, v25 op_sel:[1,0,0] op_sel_hi:[1,0,0]
	v_fma_mix_f32 v26, v59, v39, v26 op_sel_hi:[1,0,0]
	v_fma_mix_f32 v27, v59, v39, v27 op_sel:[1,0,0] op_sel_hi:[1,0,0]
	v_fma_mix_f32 v28, v60, v39, v28 op_sel_hi:[1,0,0]
	v_fma_mix_f32 v29, v60, v39, v29 op_sel:[1,0,0] op_sel_hi:[1,0,0]
	v_fma_mix_f32 v30, v61, v39, v30 op_sel_hi:[1,0,0]
	v_fma_mix_f32 v31, v61, v39, v31 op_sel:[1,0,0] op_sel_hi:[1,0,0]
	s_sub_i32 s29, s29, 4
	s_branch .Lagg_B

.Lagg_B:
	s_cmp_lt_i32 s29, 1
	s_cbranch_scc1 .Lagg_epi
	s_cmp_lt_i32 s29, 3
	s_cbranch_scc1 .Lagg_B_half
	ds_swizzle_b32 v32, v5 offset:swizzle(BITMASK_PERM, "pp100")
	ds_swizzle_b32 v33, v5 offset:swizzle(BITMASK_PERM, "pp101")
	ds_swizzle_b32 v34, v5 offset:swizzle(BITMASK_PERM, "pp110")
	ds_swizzle_b32 v35, v5 offset:swizzle(BITMASK_PERM, "pp111")
	s_waitcnt lgkmcnt(0)
	v_or_b32_e32 v32, v32, v1
	v_or_b32_e32 v33, v33, v1
	v_or_b32_e32 v34, v34, v1
	v_or_b32_e32 v35, v35, v1
	global_load_ushort v36, v32, s[6:7]
	global_load_ushort v37, v33, s[6:7]
	global_load_ushort v38, v34, s[6:7]
	global_load_ushort v39, v35, s[6:7]
	v_lshlrev_b32_e32 v32, 3, v32
	v_lshlrev_b32_e32 v33, 3, v33
	v_lshlrev_b32_e32 v34, 3, v34
	v_lshlrev_b32_e32 v35, 3, v35
	global_load_dwordx4 v[40:43], v32, s[4:5]
	global_load_dwordx4 v[44:47], v33, s[4:5]
	global_load_dwordx4 v[48:51], v34, s[4:5]
	global_load_dwordx4 v[52:55], v35, s[4:5]
	s_waitcnt vmcnt(4)
	v_fma_mix_f32 v36, v36, 1.0, v9 op_sel_hi:[1,0,0]
	v_fma_mix_f32 v37, v37, 1.0, v9 op_sel_hi:[1,0,0]
	v_fma_mix_f32 v38, v38, 1.0, v9 op_sel_hi:[1,0,0]
	v_fma_mix_f32 v39, v39, 1.0, v9 op_sel_hi:[1,0,0]
	v_mul_f32_e32 v58, 0x3e4ccccd, v36
	v_mul_f32_e32 v59, 0x3e4ccccd, v37
	v_mul_f32_e32 v60, 0x3e4ccccd, v38
	v_mul_f32_e32 v61, 0x3e4ccccd, v39
	v_max_f32_e32 v36, v36, v58
	v_max_f32_e32 v37, v37, v59
	v_max_f32_e32 v38, v38, v60
	v_max_f32_e32 v39, v39, v61
	v_max3_f32 v56, v36, v37, v38
	v_max_f32_e32 v56, v56, v39
	v_sub_f32_e32 v57, v56, v13
	v_cmp_lt_f32_e32 vcc, 0x42800000, v57
	s_cmp_lg_u64 vcc, 0
	s_cbranch_scc1 .Lagg_slow_B
.Lagg_join_B:
	v_sub_f32_e32 v36, v36, v13
	v_sub_f32_e32 v37, v37, v13
	v_sub_f32_e32 v38, v38, v13
	v_sub_f32_e32 v39, v39, v13
	v_exp_f32_e32 v36, v36
	v_exp_f32_e32 v37, v37
	v_exp_f32_e32 v38, v38
	v_exp_f32_e32 v39, v39
	v_add_f32_e32 v14, v14, v36
	v_add_f32_e32 v14, v14, v37
	v_add_f32_e32 v14, v14, v38
	v_add_f32_e32 v14, v14, v39
	s_waitcnt vmcnt(3)
	v_cvt_scalef32_pk_f16_fp8 v58, v40, 1.0
	v_cvt_scalef32_pk_f16_fp8 v59, v40, 1.0 op_sel:[1,0,0]
	v_cvt_scalef32_pk_f16_fp8 v60, v41, 1.0
	v_cvt_scalef32_pk_f16_fp8 v61, v41, 1.0 op_sel:[1,0,0]
	v_fma_mix_f32 v16, v58, v36, v16 op_sel_hi:[1,0,0]
	v_fma_mix_f32 v17, v58, v36, v17 op_sel:[1,0,0] op_sel_hi:[1,0,0]
	v_fma_mix_f32 v18, v59, v36, v18 op_sel_hi:[1,0,0]
	v_fma_mix_f32 v19, v59, v36, v19 op_sel:[1,0,0] op_sel_hi:[1,0,0]
	v_fma_mix_f32 v20, v60, v36, v20 op_sel_hi:[1,0,0]
	v_fma_mix_f32 v21, v60, v36, v21 op_sel:[1,0,0] op_sel_hi:[1,0,0]
	v_fma_mix_f32 v22, v61, v36, v22 op_sel_hi:[1,0,0]
	v_fma_mix_f32 v23, v61, v36, v23 op_sel:[1,0,0] op_sel_hi:[1,0,0]
	v_cvt_scalef32_pk_f16_fp8 v58, v42, 1.0
	v_cvt_scalef32_pk_f16_fp8 v59, v42, 1.0 op_sel:[1,0,0]
	v_cvt_scalef32_pk_f16_fp8 v60, v43, 1.0
	v_cvt_scalef32_pk_f16_fp8 v61, v43, 1.0 op_sel:[1,0,0]
	v_fma_mix_f32 v24, v58, v36, v24 op_sel_hi:[1,0,0]
	v_fma_mix_f32 v25, v58, v36, v25 op_sel:[1,0,0] op_sel_hi:[1,0,0]
	v_fma_mix_f32 v26, v59, v36, v26 op_sel_hi:[1,0,0]
	v_fma_mix_f32 v27, v59, v36, v27 op_sel:[1,0,0] op_sel_hi:[1,0,0]
	v_fma_mix_f32 v28, v60, v36, v28 op_sel_hi:[1,0,0]
	v_fma_mix_f32 v29, v60, v36, v29 op_sel:[1,0,0] op_sel_hi:[1,0,0]
	v_fma_mix_f32 v30, v61, v36, v30 op_sel_hi:[1,0,0]
	v_fma_mix_f32 v31, v61, v36, v31 op_sel:[1,0,0] op_sel_hi:[1,0,0]
	s_waitcnt vmcnt(2)
	v_cvt_scalef32_pk_f16_fp8 v58, v44, 1.0
	v_cvt_scalef32_pk_f16_fp8 v59, v44, 1.0 op_sel:[1,0,0]
	v_cvt_scalef32_pk_f16_fp8 v60, v45, 1.0
	v_cvt_scalef32_pk_f16_fp8 v61, v45, 1.0 op_sel:[1,0,0]
	v_fma_mix_f32 v16, v58, v37, v16 op_sel_hi:[1,0,0]
	v_fma_mix_f32 v17, v58, v37, v17 op_sel:[1,0,0] op_sel_hi:[1,0,0]
	v_fma_mix_f32 v18, v59, v37, v18 op_sel_hi:[1,0,0]
	v_fma_mix_f32 v19, v59, v37, v19 op_sel:[1,0,0] op_sel_hi:[1,0,0]
	v_fma_mix_f32 v20, v60, v37, v20 op_sel_hi:[1,0,0]
	v_fma_mix_f32 v21, v60, v37, v21 op_sel:[1,0,0] op_sel_hi:[1,0,0]
	v_fma_mix_f32 v22, v61, v37, v22 op_sel_hi:[1,0,0]
	v_fma_mix_f32 v23, v61, v37, v23 op_sel:[1,0,0] op_sel_hi:[1,0,0]
	v_cvt_scalef32_pk_f16_fp8 v58, v46, 1.0
	v_cvt_scalef32_pk_f16_fp8 v59, v46, 1.0 op_sel:[1,0,0]
	v_cvt_scalef32_pk_f16_fp8 v60, v47, 1.0
	v_cvt_scalef32_pk_f16_fp8 v61, v47, 1.0 op_sel:[1,0,0]
	v_fma_mix_f32 v24, v58, v37, v24 op_sel_hi:[1,0,0]
	v_fma_mix_f32 v25, v58, v37, v25 op_sel:[1,0,0] op_sel_hi:[1,0,0]
	v_fma_mix_f32 v26, v59, v37, v26 op_sel_hi:[1,0,0]
	v_fma_mix_f32 v27, v59, v37, v27 op_sel:[1,0,0] op_sel_hi:[1,0,0]
	v_fma_mix_f32 v28, v60, v37, v28 op_sel_hi:[1,0,0]
	v_fma_mix_f32 v29, v60, v37, v29 op_sel:[1,0,0] op_sel_hi:[1,0,0]
	v_fma_mix_f32 v30, v61, v37, v30 op_sel_hi:[1,0,0]
	v_fma_mix_f32 v31, v61, v37, v31 op_sel:[1,0,0] op_sel_hi:[1,0,0]
	s_waitcnt vmcnt(1)
	v_cvt_scalef32_pk_f16_fp8 v58, v48, 1.0
	v_cvt_scalef32_pk_f16_fp8 v59, v48, 1.0 op_sel:[1,0,0]
	v_cvt_scalef32_pk_f16_fp8 v60, v49, 1.0
	v_cvt_scalef32_pk_f16_fp8 v61, v49, 1.0 op_sel:[1,0,0]
	v_fma_mix_f32 v16, v58, v38, v16 op_sel_hi:[1,0,0]
	v_fma_mix_f32 v17, v58, v38, v17 op_sel:[1,0,0] op_sel_hi:[1,0,0]
	v_fma_mix_f32 v18, v59, v38, v18 op_sel_hi:[1,0,0]
	v_fma_mix_f32 v19, v59, v38, v19 op_sel:[1,0,0] op_sel_hi:[1,0,0]
	v_fma_mix_f32 v20, v60, v38, v20 op_sel_hi:[1,0,0]
	v_fma_mix_f32 v21, v60, v38, v21 op_sel:[1,0,0] op_sel_hi:[1,0,0]
	v_fma_mix_f32 v22, v61, v38, v22 op_sel_hi:[1,0,0]
	v_fma_mix_f32 v23, v61, v38, v23 op_sel:[1,0,0] op_sel_hi:[1,0,0]
	v_cvt_scalef32_pk_f16_fp8 v58, v50, 1.0
	v_cvt_scalef32_pk_f16_fp8 v59, v50, 1.0 op_sel:[1,0,0]
	v_cvt_scalef32_pk_f16_fp8 v60, v51, 1.0
	v_cvt_scalef32_pk_f16_fp8 v61, v51, 1.0 op_sel:[1,0,0]
	v_fma_mix_f32 v24, v58, v38, v24 op_sel_hi:[1,0,0]
	v_fma_mix_f32 v25, v58, v38, v25 op_sel:[1,0,0] op_sel_hi:[1,0,0]
	v_fma_mix_f32 v26, v59, v38, v26 op_sel_hi:[1,0,0]
	v_fma_mix_f32 v27, v59, v38, v27 op_sel:[1,0,0] op_sel_hi:[1,0,0]
	v_fma_mix_f32 v28, v60, v38, v28 op_sel_hi:[1,0,0]
	v_fma_mix_f32 v29, v60, v38, v29 op_sel:[1,0,0] op_sel_hi:[1,0,0]
	v_fma_mix_f32 v30, v61, v38, v30 op_sel_hi:[1,0,0]
	v_fma_mix_f32 v31, v61, v38, v31 op_sel:[1,0,0] op_sel_hi:[1,0,0]
	s_waitcnt vmcnt(0)
	v_cvt_scalef32_pk_f16_fp8 v58, v52, 1.0
	v_cvt_scalef32_pk_f16_fp8 v59, v52, 1.0 op_sel:[1,0,0]
	v_cvt_scalef32_pk_f16_fp8 v60, v53, 1.0
	v_cvt_scalef32_pk_f16_fp8 v61, v53, 1.0 op_sel:[1,0,0]
	v_fma_mix_f32 v16, v58, v39, v16 op_sel_hi:[1,0,0]
	v_fma_mix_f32 v17, v58, v39, v17 op_sel:[1,0,0] op_sel_hi:[1,0,0]
	v_fma_mix_f32 v18, v59, v39, v18 op_sel_hi:[1,0,0]
	v_fma_mix_f32 v19, v59, v39, v19 op_sel:[1,0,0] op_sel_hi:[1,0,0]
	v_fma_mix_f32 v20, v60, v39, v20 op_sel_hi:[1,0,0]
	v_fma_mix_f32 v21, v60, v39, v21 op_sel:[1,0,0] op_sel_hi:[1,0,0]
	v_fma_mix_f32 v22, v61, v39, v22 op_sel_hi:[1,0,0]
	v_fma_mix_f32 v23, v61, v39, v23 op_sel:[1,0,0] op_sel_hi:[1,0,0]
	v_cvt_scalef32_pk_f16_fp8 v58, v54, 1.0
	v_cvt_scalef32_pk_f16_fp8 v59, v54, 1.0 op_sel:[1,0,0]
	v_cvt_scalef32_pk_f16_fp8 v60, v55, 1.0
	v_cvt_scalef32_pk_f16_fp8 v61, v55, 1.0 op_sel:[1,0,0]
	v_fma_mix_f32 v24, v58, v39, v24 op_sel_hi:[1,0,0]
	v_fma_mix_f32 v25, v58, v39, v25 op_sel:[1,0,0] op_sel_hi:[1,0,0]
	v_fma_mix_f32 v26, v59, v39, v26 op_sel_hi:[1,0,0]
	v_fma_mix_f32 v27, v59, v39, v27 op_sel:[1,0,0] op_sel_hi:[1,0,0]
	v_fma_mix_f32 v28, v60, v39, v28 op_sel_hi:[1,0,0]
	v_fma_mix_f32 v29, v60, v39, v29 op_sel:[1,0,0] op_sel_hi:[1,0,0]
	v_fma_mix_f32 v30, v61, v39, v30 op_sel_hi:[1,0,0]
	v_fma_mix_f32 v31, v61, v39, v31 op_sel:[1,0,0] op_sel_hi:[1,0,0]
	s_sub_i32 s29, s29, 4
	v_mov_b32_e32 v5, v6
	v_mov_b32_e32 v6, v7
	v_mov_b32_e32 v7, v8
	v_mov_b32_e32 v8, v69
	s_add_i32 s43, s43, 1
	s_cmp_lt_i32 s29, 1
	s_cbranch_scc1 .Lagg_epi
	s_cmp_lg_u32 s43, 5
	s_cbranch_scc1 .Lagg_A
	s_add_i32 s42, s42, 40
	s_mov_b32 s43, 0
	v_add_u32_e32 v68, s42, v64
	v_add_u32_e32 v67, v10, v68
	v_lshlrev_b32_e32 v67, 2, v67
	v_mov_b32_e32 v5, s24
	v_mov_b32_e32 v6, s24
	v_mov_b32_e32 v7, s24
	v_mov_b32_e32 v8, s24
	v_mov_b32_e32 v69, s24
	v_cmp_gt_i32_e32 vcc, v11, v68
	s_and_saveexec_b64 s[32:33], vcc
	global_load_dword v5, v67, s[12:13] offset:-4
	s_mov_b64 exec, s[32:33]
	v_add_u32_e32 v68, 8, v68
	v_cmp_gt_i32_e32 vcc, v11, v68
	s_and_saveexec_b64 s[32:33], vcc
	global_load_dword v6, v67, s[12:13] offset:28
	s_mov_b64 exec, s[32:33]
	v_add_u32_e32 v68, 8, v68
	v_cmp_gt_i32_e32 vcc, v11, v68
	s_and_saveexec_b64 s[32:33], vcc
	global_load_dword v7, v67, s[12:13] offset:60
	s_mov_b64 exec, s[32:33]
	v_add_u32_e32 v68, 8, v68
	v_cmp_gt_i32_e32 vcc, v11, v68
	s_and_saveexec_b64 s[32:33], vcc
	global_load_dword v8, v67, s[12:13] offset:92
	s_mov_b64 exec, s[32:33]
	v_add_u32_e32 v68, 8, v68
	v_cmp_gt_i32_e32 vcc, v11, v68
	s_and_saveexec_b64 s[32:33], vcc
	global_load_dword v69, v67, s[12:13] offset:124
	s_mov_b64 exec, s[32:33]
	s_waitcnt vmcnt(0)
	v_lshlrev_b32_e32 v5, 4, v5
	v_lshlrev_b32_e32 v6, 4, v6
	v_lshlrev_b32_e32 v7, 4, v7
	v_lshlrev_b32_e32 v8, 4, v8
	v_lshlrev_b32_e32 v69, 4, v69
.Lagg_A:
	s_cmp_lt_i32 s29, 3
	s_cbranch_scc1 .Lagg_A_half
	ds_swizzle_b32 v32, v5 offset:swizzle(BITMASK_PERM, "pp000")
	ds_swizzle_b32 v33, v5 offset:swizzle(BITMASK_PERM, "pp001")
	ds_swizzle_b32 v34, v5 offset:swizzle(BITMASK_PERM, "pp010")
	ds_swizzle_b32 v35, v5 offset:swizzle(BITMASK_PERM, "pp011")
	s_waitcnt lgkmcnt(0)
	v_or_b32_e32 v32, v32, v1
	v_or_b32_e32 v33, v33, v1
	v_or_b32_e32 v34, v34, v1
	v_or_b32_e32 v35, v35, v1
	global_load_ushort v36, v32, s[6:7]
	global_load_ushort v37, v33, s[6:7]
	global_load_ushort v38, v34, s[6:7]
	global_load_ushort v39, v35, s[6:7]
	v_lshlrev_b32_e32 v32, 3, v32
	v_lshlrev_b32_e32 v33, 3, v33
	v_lshlrev_b32_e32 v34, 3, v34
	v_lshlrev_b32_e32 v35, 3, v35
	global_load_dwordx4 v[40:43], v32, s[4:5]
	global_load_dwordx4 v[44:47], v33, s[4:5]
	global_load_dwordx4 v[48:51], v34, s[4:5]
	global_load_dwordx4 v[52:55], v35, s[4:5]
	s_waitcnt vmcnt(4)
	v_fma_mix_f32 v36, v36, 1.0, v9 op_sel_hi:[1,0,0]
	v_fma_mix_f32 v37, v37, 1.0, v9 op_sel_hi:[1,0,0]
	v_fma_mix_f32 v38, v38, 1.0, v9 op_sel_hi:[1,0,0]
	v_fma_mix_f32 v39, v39, 1.0, v9 op_sel_hi:[1,0,0]
	v_mul_f32_e32 v58, 0x3e4ccccd, v36
	v_mul_f32_e32 v59, 0x3e4ccccd, v37
	v_mul_f32_e32 v60, 0x3e4ccccd, v38
	v_mul_f32_e32 v61, 0x3e4ccccd, v39
	v_max_f32_e32 v36, v36, v58
	v_max_f32_e32 v37, v37, v59
	v_max_f32_e32 v38, v38, v60
	v_max_f32_e32 v39, v39, v61
	v_max3_f32 v56, v36, v37, v38
	v_max_f32_e32 v56, v56, v39
	v_sub_f32_e32 v57, v56, v13
	v_cmp_lt_f32_e32 vcc, 0x42800000, v57
	s_cmp_lg_u64 vcc, 0
	s_cbranch_scc1 .Lagg_slow_A
.Lagg_join_A:
	v_sub_f32_e32 v36, v36, v13
	v_sub_f32_e32 v37, v37, v13
	v_sub_f32_e32 v38, v38, v13
	v_sub_f32_e32 v39, v39, v13
	v_exp_f32_e32 v36, v36
	v_exp_f32_e32 v37, v37
	v_exp_f32_e32 v38, v38
	v_exp_f32_e32 v39, v39
	v_add_f32_e32 v14, v14, v36
	v_add_f32_e32 v14, v14, v37
	v_add_f32_e32 v14, v14, v38
	v_add_f32_e32 v14, v14, v39
	s_waitcnt vmcnt(3)
	v_cvt_scalef32_pk_f16_fp8 v58, v40, 1.0
	v_cvt_scalef32_pk_f16_fp8 v59, v40, 1.0 op_sel:[1,0,0]
	v_cvt_scalef32_pk_f16_fp8 v60, v41, 1.0
	v_cvt_scalef32_pk_f16_fp8 v61, v41, 1.0 op_sel:[1,0,0]
	v_fma_mix_f32 v16, v58, v36, v16 op_sel_hi:[1,0,0]
	v_fma_mix_f32 v17, v58, v36, v17 op_sel:[1,0,0] op_sel_hi:[1,0,0]
	v_fma_mix_f32 v18, v59, v36, v18 op_sel_hi:[1,0,0]
	v_fma_mix_f32 v19, v59, v36, v19 op_sel:[1,0,0] op_sel_hi:[1,0,0]
	v_fma_mix_f32 v20, v60, v36, v20 op_sel_hi:[1,0,0]
	v_fma_mix_f32 v21, v60, v36, v21 op_sel:[1,0,0] op_sel_hi:[1,0,0]
	v_fma_mix_f32 v22, v61, v36, v22 op_sel_hi:[1,0,0]
	v_fma_mix_f32 v23, v61, v36, v23 op_sel:[1,0,0] op_sel_hi:[1,0,0]
	v_cvt_scalef32_pk_f16_fp8 v58, v42, 1.0
	v_cvt_scalef32_pk_f16_fp8 v59, v42, 1.0 op_sel:[1,0,0]
	v_cvt_scalef32_pk_f16_fp8 v60, v43, 1.0
	v_cvt_scalef32_pk_f16_fp8 v61, v43, 1.0 op_sel:[1,0,0]
	v_fma_mix_f32 v24, v58, v36, v24 op_sel_hi:[1,0,0]
	v_fma_mix_f32 v25, v58, v36, v25 op_sel:[1,0,0] op_sel_hi:[1,0,0]
	v_fma_mix_f32 v26, v59, v36, v26 op_sel_hi:[1,0,0]
	v_fma_mix_f32 v27, v59, v36, v27 op_sel:[1,0,0] op_sel_hi:[1,0,0]
	v_fma_mix_f32 v28, v60, v36, v28 op_sel_hi:[1,0,0]
	v_fma_mix_f32 v29, v60, v36, v29 op_sel:[1,0,0] op_sel_hi:[1,0,0]
	v_fma_mix_f32 v30, v61, v36, v30 op_sel_hi:[1,0,0]
	v_fma_mix_f32 v31, v61, v36, v31 op_sel:[1,0,0] op_sel_hi:[1,0,0]
	s_waitcnt vmcnt(2)
	v_cvt_scalef32_pk_f16_fp8 v58, v44, 1.0
	v_cvt_scalef32_pk_f16_fp8 v59, v44, 1.0 op_sel:[1,0,0]
	v_cvt_scalef32_pk_f16_fp8 v60, v45, 1.0
	v_cvt_scalef32_pk_f16_fp8 v61, v45, 1.0 op_sel:[1,0,0]
	v_fma_mix_f32 v16, v58, v37, v16 op_sel_hi:[1,0,0]
	v_fma_mix_f32 v17, v58, v37, v17 op_sel:[1,0,0] op_sel_hi:[1,0,0]
	v_fma_mix_f32 v18, v59, v37, v18 op_sel_hi:[1,0,0]
	v_fma_mix_f32 v19, v59, v37, v19 op_sel:[1,0,0] op_sel_hi:[1,0,0]
	v_fma_mix_f32 v20, v60, v37, v20 op_sel_hi:[1,0,0]
	v_fma_mix_f32 v21, v60, v37, v21 op_sel:[1,0,0] op_sel_hi:[1,0,0]
	v_fma_mix_f32 v22, v61, v37, v22 op_sel_hi:[1,0,0]
	v_fma_mix_f32 v23, v61, v37, v23 op_sel:[1,0,0] op_sel_hi:[1,0,0]
	v_cvt_scalef32_pk_f16_fp8 v58, v46, 1.0
	v_cvt_scalef32_pk_f16_fp8 v59, v46, 1.0 op_sel:[1,0,0]
	v_cvt_scalef32_pk_f16_fp8 v60, v47, 1.0
	v_cvt_scalef32_pk_f16_fp8 v61, v47, 1.0 op_sel:[1,0,0]
	v_fma_mix_f32 v24, v58, v37, v24 op_sel_hi:[1,0,0]
	v_fma_mix_f32 v25, v58, v37, v25 op_sel:[1,0,0] op_sel_hi:[1,0,0]
	v_fma_mix_f32 v26, v59, v37, v26 op_sel_hi:[1,0,0]
	v_fma_mix_f32 v27, v59, v37, v27 op_sel:[1,0,0] op_sel_hi:[1,0,0]
	v_fma_mix_f32 v28, v60, v37, v28 op_sel_hi:[1,0,0]
	v_fma_mix_f32 v29, v60, v37, v29 op_sel:[1,0,0] op_sel_hi:[1,0,0]
	v_fma_mix_f32 v30, v61, v37, v30 op_sel_hi:[1,0,0]
	v_fma_mix_f32 v31, v61, v37, v31 op_sel:[1,0,0] op_sel_hi:[1,0,0]
	s_waitcnt vmcnt(1)
	v_cvt_scalef32_pk_f16_fp8 v58, v48, 1.0
	v_cvt_scalef32_pk_f16_fp8 v59, v48, 1.0 op_sel:[1,0,0]
	v_cvt_scalef32_pk_f16_fp8 v60, v49, 1.0
	v_cvt_scalef32_pk_f16_fp8 v61, v49, 1.0 op_sel:[1,0,0]
	v_fma_mix_f32 v16, v58, v38, v16 op_sel_hi:[1,0,0]
	v_fma_mix_f32 v17, v58, v38, v17 op_sel:[1,0,0] op_sel_hi:[1,0,0]
	v_fma_mix_f32 v18, v59, v38, v18 op_sel_hi:[1,0,0]
	v_fma_mix_f32 v19, v59, v38, v19 op_sel:[1,0,0] op_sel_hi:[1,0,0]
	v_fma_mix_f32 v20, v60, v38, v20 op_sel_hi:[1,0,0]
	v_fma_mix_f32 v21, v60, v38, v21 op_sel:[1,0,0] op_sel_hi:[1,0,0]
	v_fma_mix_f32 v22, v61, v38, v22 op_sel_hi:[1,0,0]
	v_fma_mix_f32 v23, v61, v38, v23 op_sel:[1,0,0] op_sel_hi:[1,0,0]
	v_cvt_scalef32_pk_f16_fp8 v58, v50, 1.0
	v_cvt_scalef32_pk_f16_fp8 v59, v50, 1.0 op_sel:[1,0,0]
	v_cvt_scalef32_pk_f16_fp8 v60, v51, 1.0
	v_cvt_scalef32_pk_f16_fp8 v61, v51, 1.0 op_sel:[1,0,0]
	v_fma_mix_f32 v24, v58, v38, v24 op_sel_hi:[1,0,0]
	v_fma_mix_f32 v25, v58, v38, v25 op_sel:[1,0,0] op_sel_hi:[1,0,0]
	v_fma_mix_f32 v26, v59, v38, v26 op_sel_hi:[1,0,0]
	v_fma_mix_f32 v27, v59, v38, v27 op_sel:[1,0,0] op_sel_hi:[1,0,0]
	v_fma_mix_f32 v28, v60, v38, v28 op_sel_hi:[1,0,0]
	v_fma_mix_f32 v29, v60, v38, v29 op_sel:[1,0,0] op_sel_hi:[1,0,0]
	v_fma_mix_f32 v30, v61, v38, v30 op_sel_hi:[1,0,0]
	v_fma_mix_f32 v31, v61, v38, v31 op_sel:[1,0,0] op_sel_hi:[1,0,0]
	s_waitcnt vmcnt(0)
	v_cvt_scalef32_pk_f16_fp8 v58, v52, 1.0
	v_cvt_scalef32_pk_f16_fp8 v59, v52, 1.0 op_sel:[1,0,0]
	v_cvt_scalef32_pk_f16_fp8 v60, v53, 1.0
	v_cvt_scalef32_pk_f16_fp8 v61, v53, 1.0 op_sel:[1,0,0]
	v_fma_mix_f32 v16, v58, v39, v16 op_sel_hi:[1,0,0]
	v_fma_mix_f32 v17, v58, v39, v17 op_sel:[1,0,0] op_sel_hi:[1,0,0]
	v_fma_mix_f32 v18, v59, v39, v18 op_sel_hi:[1,0,0]
	v_fma_mix_f32 v19, v59, v39, v19 op_sel:[1,0,0] op_sel_hi:[1,0,0]
	v_fma_mix_f32 v20, v60, v39, v20 op_sel_hi:[1,0,0]
	v_fma_mix_f32 v21, v60, v39, v21 op_sel:[1,0,0] op_sel_hi:[1,0,0]
	v_fma_mix_f32 v22, v61, v39, v22 op_sel_hi:[1,0,0]
	v_fma_mix_f32 v23, v61, v39, v23 op_sel:[1,0,0] op_sel_hi:[1,0,0]
	v_cvt_scalef32_pk_f16_fp8 v58, v54, 1.0
	v_cvt_scalef32_pk_f16_fp8 v59, v54, 1.0 op_sel:[1,0,0]
	v_cvt_scalef32_pk_f16_fp8 v60, v55, 1.0
	v_cvt_scalef32_pk_f16_fp8 v61, v55, 1.0 op_sel:[1,0,0]
	v_fma_mix_f32 v24, v58, v39, v24 op_sel_hi:[1,0,0]
	v_fma_mix_f32 v25, v58, v39, v25 op_sel:[1,0,0] op_sel_hi:[1,0,0]
	v_fma_mix_f32 v26, v59, v39, v26 op_sel_hi:[1,0,0]
	v_fma_mix_f32 v27, v59, v39, v27 op_sel:[1,0,0] op_sel_hi:[1,0,0]
	v_fma_mix_f32 v28, v60, v39, v28 op_sel_hi:[1,0,0]
	v_fma_mix_f32 v29, v60, v39, v29 op_sel:[1,0,0] op_sel_hi:[1,0,0]
	v_fma_mix_f32 v30, v61, v39, v30 op_sel_hi:[1,0,0]
	v_fma_mix_f32 v31, v61, v39, v31 op_sel:[1,0,0] op_sel_hi:[1,0,0]
	s_sub_i32 s29, s29, 4
	s_branch .Lagg_B
.Lagg_A_half:
	ds_swizzle_b32 v32, v5 offset:swizzle(BITMASK_PERM, "pp000")
	ds_swizzle_b32 v33, v5 offset:swizzle(BITMASK_PERM, "pp001")
	s_waitcnt lgkmcnt(0)
	v_or_b32_e32 v32, v32, v1
	v_or_b32_e32 v33, v33, v1
	global_load_ushort v36, v32, s[6:7]
	global_load_ushort v37, v33, s[6:7]
	v_lshlrev_b32_e32 v32, 3, v32
	v_lshlrev_b32_e32 v33, 3, v33
	global_load_dwordx4 v[40:43], v32, s[4:5]
	global_load_dwordx4 v[44:47], v33, s[4:5]
	s_waitcnt vmcnt(2)
	v_fma_mix_f32 v36, v36, 1.0, v9 op_sel_hi:[1,0,0]
	v_fma_mix_f32 v37, v37, 1.0, v9 op_sel_hi:[1,0,0]
	v_mul_f32_e32 v58, 0x3e4ccccd, v36
	v_mul_f32_e32 v59, 0x3e4ccccd, v37
	v_max_f32_e32 v36, v36, v58
	v_max_f32_e32 v37, v37, v59
	v_max_f32_e32 v56, v36, v37
	v_sub_f32_e32 v57, v56, v13
	v_cmp_lt_f32_e32 vcc, 0x42800000, v57
	s_cmp_lg_u64 vcc, 0
	s_cbranch_scc1 .Lagg_slow_Ah
.Lagg_join_Ah:
	v_sub_f32_e32 v36, v36, v13
	v_sub_f32_e32 v37, v37, v13
	v_exp_f32_e32 v36, v36
	v_exp_f32_e32 v37, v37
	v_add_f32_e32 v14, v14, v36
	v_add_f32_e32 v14, v14, v37
	s_waitcnt vmcnt(1)
	v_cvt_scalef32_pk_f16_fp8 v58, v40, 1.0
	v_cvt_scalef32_pk_f16_fp8 v59, v40, 1.0 op_sel:[1,0,0]
	v_cvt_scalef32_pk_f16_fp8 v60, v41, 1.0
	v_cvt_scalef32_pk_f16_fp8 v61, v41, 1.0 op_sel:[1,0,0]
	v_fma_mix_f32 v16, v58, v36, v16 op_sel_hi:[1,0,0]
	v_fma_mix_f32 v17, v58, v36, v17 op_sel:[1,0,0] op_sel_hi:[1,0,0]
	v_fma_mix_f32 v18, v59, v36, v18 op_sel_hi:[1,0,0]
	v_fma_mix_f32 v19, v59, v36, v19 op_sel:[1,0,0] op_sel_hi:[1,0,0]
	v_fma_mix_f32 v20, v60, v36, v20 op_sel_hi:[1,0,0]
	v_fma_mix_f32 v21, v60, v36, v21 op_sel:[1,0,0] op_sel_hi:[1,0,0]
	v_fma_mix_f32 v22, v61, v36, v22 op_sel_hi:[1,0,0]
	v_fma_mix_f32 v23, v61, v36, v23 op_sel:[1,0,0] op_sel_hi:[1,0,0]
	v_cvt_scalef32_pk_f16_fp8 v58, v42, 1.0
	v_cvt_scalef32_pk_f16_fp8 v59, v42, 1.0 op_sel:[1,0,0]
	v_cvt_scalef32_pk_f16_fp8 v60, v43, 1.0
	v_cvt_scalef32_pk_f16_fp8 v61, v43, 1.0 op_sel:[1,0,0]
	v_fma_mix_f32 v24, v58, v36, v24 op_sel_hi:[1,0,0]
	v_fma_mix_f32 v25, v58, v36, v25 op_sel:[1,0,0] op_sel_hi:[1,0,0]
	v_fma_mix_f32 v26, v59, v36, v26 op_sel_hi:[1,0,0]
	v_fma_mix_f32 v27, v59, v36, v27 op_sel:[1,0,0] op_sel_hi:[1,0,0]
	v_fma_mix_f32 v28, v60, v36, v28 op_sel_hi:[1,0,0]
	v_fma_mix_f32 v29, v60, v36, v29 op_sel:[1,0,0] op_sel_hi:[1,0,0]
	v_fma_mix_f32 v30, v61, v36, v30 op_sel_hi:[1,0,0]
	v_fma_mix_f32 v31, v61, v36, v31 op_sel:[1,0,0] op_sel_hi:[1,0,0]
	s_waitcnt vmcnt(0)
	v_cvt_scalef32_pk_f16_fp8 v58, v44, 1.0
	v_cvt_scalef32_pk_f16_fp8 v59, v44, 1.0 op_sel:[1,0,0]
	v_cvt_scalef32_pk_f16_fp8 v60, v45, 1.0
	v_cvt_scalef32_pk_f16_fp8 v61, v45, 1.0 op_sel:[1,0,0]
	v_fma_mix_f32 v16, v58, v37, v16 op_sel_hi:[1,0,0]
	v_fma_mix_f32 v17, v58, v37, v17 op_sel:[1,0,0] op_sel_hi:[1,0,0]
	v_fma_mix_f32 v18, v59, v37, v18 op_sel_hi:[1,0,0]
	v_fma_mix_f32 v19, v59, v37, v19 op_sel:[1,0,0] op_sel_hi:[1,0,0]
	v_fma_mix_f32 v20, v60, v37, v20 op_sel_hi:[1,0,0]
	v_fma_mix_f32 v21, v60, v37, v21 op_sel:[1,0,0] op_sel_hi:[1,0,0]
	v_fma_mix_f32 v22, v61, v37, v22 op_sel_hi:[1,0,0]
	v_fma_mix_f32 v23, v61, v37, v23 op_sel:[1,0,0] op_sel_hi:[1,0,0]
	v_cvt_scalef32_pk_f16_fp8 v58, v46, 1.0
	v_cvt_scalef32_pk_f16_fp8 v59, v46, 1.0 op_sel:[1,0,0]
	v_cvt_scalef32_pk_f16_fp8 v60, v47, 1.0
	v_cvt_scalef32_pk_f16_fp8 v61, v47, 1.0 op_sel:[1,0,0]
	v_fma_mix_f32 v24, v58, v37, v24 op_sel_hi:[1,0,0]
	v_fma_mix_f32 v25, v58, v37, v25 op_sel:[1,0,0] op_sel_hi:[1,0,0]
	v_fma_mix_f32 v26, v59, v37, v26 op_sel_hi:[1,0,0]
	v_fma_mix_f32 v27, v59, v37, v27 op_sel:[1,0,0] op_sel_hi:[1,0,0]
	v_fma_mix_f32 v28, v60, v37, v28 op_sel_hi:[1,0,0]
	v_fma_mix_f32 v29, v60, v37, v29 op_sel:[1,0,0] op_sel_hi:[1,0,0]
	v_fma_mix_f32 v30, v61, v37, v30 op_sel_hi:[1,0,0]
	v_fma_mix_f32 v31, v61, v37, v31 op_sel:[1,0,0] op_sel_hi:[1,0,0]
	s_branch .Lagg_epi
.Lagg_B_half:
	ds_swizzle_b32 v32, v5 offset:swizzle(BITMASK_PERM, "pp100")
	ds_swizzle_b32 v33, v5 offset:swizzle(BITMASK_PERM, "pp101")
	s_waitcnt lgkmcnt(0)
	v_or_b32_e32 v32, v32, v1
	v_or_b32_e32 v33, v33, v1
	global_load_ushort v36, v32, s[6:7]
	global_load_ushort v37, v33, s[6:7]
	v_lshlrev_b32_e32 v32, 3, v32
	v_lshlrev_b32_e32 v33, 3, v33
	global_load_dwordx4 v[40:43], v32, s[4:5]
	global_load_dwordx4 v[44:47], v33, s[4:5]
	s_waitcnt vmcnt(2)
	v_fma_mix_f32 v36, v36, 1.0, v9 op_sel_hi:[1,0,0]
	v_fma_mix_f32 v37, v37, 1.0, v9 op_sel_hi:[1,0,0]
	v_mul_f32_e32 v58, 0x3e4ccccd, v36
	v_mul_f32_e32 v59, 0x3e4ccccd, v37
	v_max_f32_e32 v36, v36, v58
	v_max_f32_e32 v37, v37, v59
	v_max_f32_e32 v56, v36, v37
	v_sub_f32_e32 v57, v56, v13
	v_cmp_lt_f32_e32 vcc, 0x42800000, v57
	s_cmp_lg_u64 vcc, 0
	s_cbranch_scc1 .Lagg_slow_Bh
.Lagg_join_Bh:
	v_sub_f32_e32 v36, v36, v13
	v_sub_f32_e32 v37, v37, v13
	v_exp_f32_e32 v36, v36
	v_exp_f32_e32 v37, v37
	v_add_f32_e32 v14, v14, v36
	v_add_f32_e32 v14, v14, v37
	s_waitcnt vmcnt(1)
	v_cvt_scalef32_pk_f16_fp8 v58, v40, 1.0
	v_cvt_scalef32_pk_f16_fp8 v59, v40, 1.0 op_sel:[1,0,0]
	v_cvt_scalef32_pk_f16_fp8 v60, v41, 1.0
	v_cvt_scalef32_pk_f16_fp8 v61, v41, 1.0 op_sel:[1,0,0]
	v_fma_mix_f32 v16, v58, v36, v16 op_sel_hi:[1,0,0]
	v_fma_mix_f32 v17, v58, v36, v17 op_sel:[1,0,0] op_sel_hi:[1,0,0]
	v_fma_mix_f32 v18, v59, v36, v18 op_sel_hi:[1,0,0]
	v_fma_mix_f32 v19, v59, v36, v19 op_sel:[1,0,0] op_sel_hi:[1,0,0]
	v_fma_mix_f32 v20, v60, v36, v20 op_sel_hi:[1,0,0]
	v_fma_mix_f32 v21, v60, v36, v21 op_sel:[1,0,0] op_sel_hi:[1,0,0]
	v_fma_mix_f32 v22, v61, v36, v22 op_sel_hi:[1,0,0]
	v_fma_mix_f32 v23, v61, v36, v23 op_sel:[1,0,0] op_sel_hi:[1,0,0]
	v_cvt_scalef32_pk_f16_fp8 v58, v42, 1.0
	v_cvt_scalef32_pk_f16_fp8 v59, v42, 1.0 op_sel:[1,0,0]
	v_cvt_scalef32_pk_f16_fp8 v60, v43, 1.0
	v_cvt_scalef32_pk_f16_fp8 v61, v43, 1.0 op_sel:[1,0,0]
	v_fma_mix_f32 v24, v58, v36, v24 op_sel_hi:[1,0,0]
	v_fma_mix_f32 v25, v58, v36, v25 op_sel:[1,0,0] op_sel_hi:[1,0,0]
	v_fma_mix_f32 v26, v59, v36, v26 op_sel_hi:[1,0,0]
	v_fma_mix_f32 v27, v59, v36, v27 op_sel:[1,0,0] op_sel_hi:[1,0,0]
	v_fma_mix_f32 v28, v60, v36, v28 op_sel_hi:[1,0,0]
	v_fma_mix_f32 v29, v60, v36, v29 op_sel:[1,0,0] op_sel_hi:[1,0,0]
	v_fma_mix_f32 v30, v61, v36, v30 op_sel_hi:[1,0,0]
	v_fma_mix_f32 v31, v61, v36, v31 op_sel:[1,0,0] op_sel_hi:[1,0,0]
	s_waitcnt vmcnt(0)
	v_cvt_scalef32_pk_f16_fp8 v58, v44, 1.0
	v_cvt_scalef32_pk_f16_fp8 v59, v44, 1.0 op_sel:[1,0,0]
	v_cvt_scalef32_pk_f16_fp8 v60, v45, 1.0
	v_cvt_scalef32_pk_f16_fp8 v61, v45, 1.0 op_sel:[1,0,0]
	v_fma_mix_f32 v16, v58, v37, v16 op_sel_hi:[1,0,0]
	v_fma_mix_f32 v17, v58, v37, v17 op_sel:[1,0,0] op_sel_hi:[1,0,0]
	v_fma_mix_f32 v18, v59, v37, v18 op_sel_hi:[1,0,0]
	v_fma_mix_f32 v19, v59, v37, v19 op_sel:[1,0,0] op_sel_hi:[1,0,0]
	v_fma_mix_f32 v20, v60, v37, v20 op_sel_hi:[1,0,0]
	v_fma_mix_f32 v21, v60, v37, v21 op_sel:[1,0,0] op_sel_hi:[1,0,0]
	v_fma_mix_f32 v22, v61, v37, v22 op_sel_hi:[1,0,0]
	v_fma_mix_f32 v23, v61, v37, v23 op_sel:[1,0,0] op_sel_hi:[1,0,0]
	v_cvt_scalef32_pk_f16_fp8 v58, v46, 1.0
	v_cvt_scalef32_pk_f16_fp8 v59, v46, 1.0 op_sel:[1,0,0]
	v_cvt_scalef32_pk_f16_fp8 v60, v47, 1.0
	v_cvt_scalef32_pk_f16_fp8 v61, v47, 1.0 op_sel:[1,0,0]
	v_fma_mix_f32 v24, v58, v37, v24 op_sel_hi:[1,0,0]
	v_fma_mix_f32 v25, v58, v37, v25 op_sel:[1,0,0] op_sel_hi:[1,0,0]
	v_fma_mix_f32 v26, v59, v37, v26 op_sel_hi:[1,0,0]
	v_fma_mix_f32 v27, v59, v37, v27 op_sel:[1,0,0] op_sel_hi:[1,0,0]
	v_fma_mix_f32 v28, v60, v37, v28 op_sel_hi:[1,0,0]
	v_fma_mix_f32 v29, v60, v37, v29 op_sel:[1,0,0] op_sel_hi:[1,0,0]
	v_fma_mix_f32 v30, v61, v37, v30 op_sel_hi:[1,0,0]
	v_fma_mix_f32 v31, v61, v37, v31 op_sel:[1,0,0] op_sel_hi:[1,0,0]

.Lagg_slow_B:
	v_max_f32_e32 v56, v56, v13
	v_sub_f32_e32 v57, v13, v56
	v_exp_f32_e32 v57, v57
	v_mov_b32_e32 v13, v56
	v_mul_f32_e32 v14, v14, v57
	v_mul_f32_e32 v16, v16, v57
	v_mul_f32_e32 v17, v17, v57
	v_mul_f32_e32 v18, v18, v57
	v_mul_f32_e32 v19, v19, v57
	v_mul_f32_e32 v20, v20, v57
	v_mul_f32_e32 v21, v21, v57
	v_mul_f32_e32 v22, v22, v57
	v_mul_f32_e32 v23, v23, v57
	v_mul_f32_e32 v24, v24, v57
	v_mul_f32_e32 v25, v25, v57
	v_mul_f32_e32 v26, v26, v57
	v_mul_f32_e32 v27, v27, v57
	v_mul_f32_e32 v28, v28, v57
	v_mul_f32_e32 v29, v29, v57
	v_mul_f32_e32 v30, v30, v57
	v_mul_f32_e32 v31, v31, v57
	s_branch .Lagg_join_B
